# phase 10 GEMM K-loop: lane-constant clusters skipped on trips 2..8 and 14 (on top of hoists for phases 1,5,6,7,11, unscaled fp8 MFMA, NSA mask)
# baseline (speedup 1.0000x reference)
.LBB0_2454:
	s_sub_u32 s100, s77, 2
	s_cmp_lt_u32 s100, 7
	s_cselect_b32 s100, 1, 0
	s_cbranch_scc1 .Lp10_b
	s_cmp_eq_u32 s77, 14
	s_cselect_b32 s100, 1, 0
	s_cbranch_scc1 .Lp10_b
	v_mbcnt_lo_u32_b32 v4, -1, 0
	v_mbcnt_hi_u32_b32 v4, -1, v4
	s_cmp_lt_i32 s77, 12
	v_add_u32_e32 v0, s47, v4
	v_lshlrev_b32_e32 v206, 4, v0
	v_lshlrev_b32_e32 v5, 4, v4
	v_bitop3_b32 v201, v0, s48, v5 bitop3:0x48
	v_ashrrev_i32_e32 v203, 3, v0
	v_add_u32_e32 v0, 0x2000, v206
	v_ashrrev_i32_e32 v202, 7, v0
	s_mov_b64 s[10:11], -1
	s_cbranch_scc1 .LBB0_2464
	s_cmp_eq_u32 s77, 12
	s_mov_b64 s[6:7], s[34:35]
	s_mov_b32 s14, s46
	s_mov_b32 s15, s44
	s_mov_b32 s84, s43
	s_mov_b32 s83, s45
	s_cbranch_scc0 .LBB0_2463
	v_cndmask_b32_e64 v0, 0, 1, s[38:39]
	v_cmp_ne_u32_e64 s[6:7], 1, v0
	s_andn2_b64 vcc, exec, s[38:39]
	s_mov_b32 s14, s76
	s_mov_b32 s83, s45
	s_mov_b32 s84, s43
	s_mov_b32 s15, s44
	s_cbranch_vccz .LBB0_2475
	s_and_b64 vcc, exec, s[6:7]
	v_mov_b32_e32 v0, v64
	s_cbranch_vccz .LBB0_2476

.LBB0_2471:
	v_and_b32_e32 v0, 15, v4
	v_lshrrev_b32_e32 v2, 3, v4
	v_bfe_u32 v4, v4, 1, 3
	s_mov_b32 s6, 0xffffffe
	v_lshlrev_b32_e32 v0, 7, v0
	v_and_b32_e32 v3, 0xffffffe, v2
	v_bitop3_b32 v2, v2, v4, s6 bitop3:0x6c
	v_or_b32_e32 v1, s64, v0
	v_or_b32_e32 v0, s65, v0
	v_lshlrev_b32_e32 v2, 4, v2
	v_add_u32_e32 v32, v2, v1
	v_add_u32_e32 v204, v2, v0
	v_bitop3_b32 v2, v3, v4, 1 bitop3:0x36
	v_lshlrev_b32_e32 v2, 4, v2
	v_add_u32_e32 v205, v2, v0
	v_add_u32_e32 v33, v2, v1
	v_add_u32_e32 v200, 0, v32
	v_add_u32_e32 v199, 0, v33
.Lp10_b:
	v_add_u32_e32 v0, s70, v204
	v_add_u32_e32 v1, s70, v205
	v_add_u32_e32 v4, s71, v204
	v_add_u32_e32 v12, s71, v205
	ds_read_b128 v[16:19], v0
	ds_read_b128 v[24:27], v0 offset:2048
	ds_read_b128 v[20:23], v1
	ds_read_b128 v[28:31], v1 offset:2048
	ds_read_b128 v[0:3], v4
	ds_read_b128 v[8:11], v4 offset:2048
	ds_read_b128 v[4:7], v12
	ds_read_b128 v[12:15], v12 offset:2048
	s_cmp_eq_u32 s77, 14
	s_cselect_b64 s[6:7], -1, 0
	s_add_i32 s10, s82, 0xffffff00
	s_cmp_lg_u32 s77, 14
	s_mov_b32 m0, s66
	ds_read_b128 v[40:43], v200
	ds_read_b128 v[32:35], v200 offset:2048
	ds_read_b128 v[44:47], v199
	ds_read_b128 v[36:39], v199 offset:2048
	ds_read_b128 v[56:59], v200 offset:4096
	ds_read_b128 v[48:51], v200 offset:6144
	ds_read_b128 v[60:63], v199 offset:4096
	ds_read_b128 v[52:55], v199 offset:6144
	buffer_load_dwordx4 v66, s[16:19], s10 offen lds
	s_mov_b32 m0, s69
	s_nop 0
	buffer_load_dwordx4 v67, s[16:19], s10 offen lds
	s_cbranch_scc1 .LBB0_2473
	v_mbcnt_lo_u32_b32 v64, -1, 0
	v_mbcnt_hi_u32_b32 v64, -1, v64
	v_add_u32_e32 v64, s47, v64
	v_lshlrev_b32_e32 v64, 4, v64
	v_add_u32_e32 v64, 0x20000, v64
	ds_read_b128 v[64:67], v64
.LBB0_2473:
	s_cmp_lg_u32 s100, 0
	s_cbranch_scc1 .Lp10_c
	v_lshlrev_b32_e32 v206, 1, v203
	v_lshrrev_b32_e32 v207, 2, v203
	v_and_b32_e32 v206, 24, v206
	v_and_b32_e32 v207, 4, v207
	v_and_b32_e32 v203, 0x1fffe3, v203
	v_or3_b32 v203, v203, v207, v206
	v_lshlrev_b32_e32 v206, 1, v202
	v_lshrrev_b32_e32 v207, 2, v202
	v_and_b32_e32 v206, 24, v206
	v_and_b32_e32 v207, 4, v207
	v_and_b32_e32 v202, 0x1fffe3, v202
	v_or3_b32 v202, v202, v207, v206
	v_lshl_or_b32 v203, v203, 11, v201
	v_lshl_or_b32 v201, v202, 11, v201
.Lp10_c:
	s_add_i32 s10, s82, 0xffffff80
	s_waitcnt vmcnt(8)
	s_add_i32 s14, s77, 2
	s_add_i32 s11, s10, s76
	s_waitcnt lgkmcnt(0)
	s_and_b64 s[6:7], s[6:7], exec
	s_cselect_b32 s7, s46, s11
	s_cselect_b32 s6, 0x80, s82
	s_cselect_b32 s83, 0, s10
	s_add_i32 s15, s7, 0x80
	s_barrier
	s_setprio 1
	s_waitcnt lgkmcnt(0)
	v_mfma_f32_16x16x128_f8f6f4 v[192:195], v[16:23], v[40:47], v[192:195]
	v_mfma_f32_16x16x128_f8f6f4 v[188:191], v[24:31], v[40:47], v[188:191]
	v_mfma_f32_16x16x128_f8f6f4 v[176:179], v[16:23], v[32:39], v[176:179]
	v_mfma_f32_16x16x128_f8f6f4 v[168:171], v[24:31], v[32:39], v[168:171]
	v_mfma_f32_16x16x128_f8f6f4 v[160:163], v[16:23], v[56:63], v[160:163]
	v_mfma_f32_16x16x128_f8f6f4 v[152:155], v[24:31], v[56:63], v[152:155]
	v_mfma_f32_16x16x128_f8f6f4 v[144:147], v[16:23], v[48:55], v[144:147]
	v_mfma_f32_16x16x128_f8f6f4 v[136:139], v[24:31], v[48:55], v[136:139]
	s_setprio 0
	s_setprio 1
	v_mfma_f32_16x16x128_f8f6f4 v[184:187], v[0:7], v[40:47], v[184:187]
	v_mfma_f32_16x16x128_f8f6f4 v[180:183], v[8:15], v[40:47], v[180:183]
	v_mfma_f32_16x16x128_f8f6f4 v[172:175], v[0:7], v[32:39], v[172:175]
	v_mfma_f32_16x16x128_f8f6f4 v[164:167], v[8:15], v[32:39], v[164:167]
	v_mfma_f32_16x16x128_f8f6f4 v[156:159], v[0:7], v[56:63], v[156:159]
	v_mfma_f32_16x16x128_f8f6f4 v[148:151], v[8:15], v[56:63], v[148:151]
	v_mfma_f32_16x16x128_f8f6f4 v[140:143], v[0:7], v[48:55], v[140:143]
	v_mfma_f32_16x16x128_f8f6f4 v[132:135], v[8:15], v[48:55], v[132:135]
	s_setprio 0
	s_barrier
	s_mov_b32 m0, s50
	s_mov_b32 s10, s18
	s_mov_b32 s11, s19
	ds_read_b128 v[32:35], v200 offset:16384
	ds_read_b128 v[40:43], v200 offset:18432
	ds_read_b128 v[36:39], v199 offset:16384
	ds_read_b128 v[44:47], v199 offset:18432
	ds_read_b128 v[48:51], v200 offset:20480
	ds_read_b128 v[56:59], v200 offset:22528
	ds_read_b128 v[52:55], v199 offset:20480
	ds_read_b128 v[60:63], v199 offset:22528
	buffer_load_dwordx4 v203, s[8:11], s7 offen lds
	s_mov_b32 m0, s51
	s_add_i32 s84, s7, 0x40000
	buffer_load_dwordx4 v201, s[8:11], s7 offen lds
	s_mov_b32 m0, s52
	s_nop 0
	buffer_load_dwordx4 v203, s[8:11], s84 offen lds
	s_mov_b32 m0, s53
	s_nop 0
	buffer_load_dwordx4 v201, s[8:11], s84 offen lds
	s_mov_b32 m0, s49
	s_nop 0
	buffer_load_dwordx4 v64, s[16:19], s83 offen lds
	s_mov_b32 m0, s54
	s_nop 0
	buffer_load_dwordx4 v65, s[16:19], s83 offen lds
	s_waitcnt vmcnt(8)
	s_waitcnt lgkmcnt(0)
	s_barrier
	s_setprio 1
	s_waitcnt lgkmcnt(5)
	v_mfma_f32_16x16x128_f8f6f4 v[128:131], v[16:23], v[32:39], v[128:131]
	v_mfma_f32_16x16x128_f8f6f4 v[120:123], v[24:31], v[32:39], v[120:123]
	s_waitcnt lgkmcnt(4)
	v_mfma_f32_16x16x128_f8f6f4 v[112:115], v[16:23], v[40:47], v[112:115]
	v_mfma_f32_16x16x128_f8f6f4 v[104:107], v[24:31], v[40:47], v[104:107]
	s_waitcnt lgkmcnt(1)
	v_mfma_f32_16x16x128_f8f6f4 v[96:99], v[16:23], v[48:55], v[96:99]
	v_mfma_f32_16x16x128_f8f6f4 v[88:91], v[24:31], v[48:55], v[88:91]
	s_waitcnt lgkmcnt(0)
	v_mfma_f32_16x16x128_f8f6f4 v[80:83], v[16:23], v[56:63], v[80:83]
	v_mfma_f32_16x16x128_f8f6f4 v[72:75], v[24:31], v[56:63], v[72:75]
	s_setprio 0
	s_setprio 1
	v_mfma_f32_16x16x128_f8f6f4 v[124:127], v[0:7], v[32:39], v[124:127]
	v_mfma_f32_16x16x128_f8f6f4 v[116:119], v[8:15], v[32:39], v[116:119]
	v_mfma_f32_16x16x128_f8f6f4 v[108:111], v[0:7], v[40:47], v[108:111]
	v_mfma_f32_16x16x128_f8f6f4 v[100:103], v[8:15], v[40:47], v[100:103]
	v_mfma_f32_16x16x128_f8f6f4 v[92:95], v[0:7], v[48:55], v[92:95]
	v_mfma_f32_16x16x128_f8f6f4 v[84:87], v[8:15], v[48:55], v[84:87]
	v_mfma_f32_16x16x128_f8f6f4 v[76:79], v[0:7], v[56:63], v[76:79]
	v_mfma_f32_16x16x128_f8f6f4 v[68:71], v[8:15], v[56:63], v[68:71]
	s_setprio 0
	s_barrier
	s_add_i32 s84, 0, 0x18000
	v_add_u32_e32 v4, s84, v204
	v_add_u32_e32 v12, s84, v205
	s_add_i32 s84, 0, 0x1c000
	v_add_u32_e32 v20, s84, v204
	v_add_u32_e32 v28, s84, v205
	ds_read_b128 v[0:3], v4
	ds_read_b128 v[8:11], v4 offset:2048
	ds_read_b128 v[4:7], v12
	ds_read_b128 v[12:15], v12 offset:2048
	ds_read_b128 v[16:19], v20
	ds_read_b128 v[24:27], v20 offset:2048
	ds_read_b128 v[20:23], v28
	ds_read_b128 v[28:31], v28 offset:2048
	s_mov_b32 m0, s55
	ds_read_b128 v[32:35], v200 offset:32768
	ds_read_b128 v[40:43], v200 offset:34816
	ds_read_b128 v[36:39], v199 offset:32768
	ds_read_b128 v[44:47], v199 offset:34816
	ds_read_b128 v[48:51], v200 offset:36864
	ds_read_b128 v[56:59], v200 offset:38912
	ds_read_b128 v[52:55], v199 offset:36864
	ds_read_b128 v[60:63], v199 offset:38912
	buffer_load_dwordx4 v66, s[16:19], s83 offen lds
	s_mov_b32 m0, s56
	s_nop 0
	buffer_load_dwordx4 v67, s[16:19], s83 offen lds
	s_waitcnt vmcnt(8)
	s_waitcnt lgkmcnt(0)
	s_barrier
	s_setprio 1
	s_waitcnt lgkmcnt(5)
	v_mfma_f32_16x16x128_f8f6f4 v[192:195], v[0:7], v[32:39], v[192:195]
	v_mfma_f32_16x16x128_f8f6f4 v[188:191], v[8:15], v[32:39], v[188:191]
	s_waitcnt lgkmcnt(4)
	v_mfma_f32_16x16x128_f8f6f4 v[176:179], v[0:7], v[40:47], v[176:179]
	v_mfma_f32_16x16x128_f8f6f4 v[168:171], v[8:15], v[40:47], v[168:171]
	s_waitcnt lgkmcnt(1)
	v_mfma_f32_16x16x128_f8f6f4 v[160:163], v[0:7], v[48:55], v[160:163]
	v_mfma_f32_16x16x128_f8f6f4 v[152:155], v[8:15], v[48:55], v[152:155]
	s_waitcnt lgkmcnt(0)
	v_mfma_f32_16x16x128_f8f6f4 v[144:147], v[0:7], v[56:63], v[144:147]
	v_mfma_f32_16x16x128_f8f6f4 v[136:139], v[8:15], v[56:63], v[136:139]
	s_setprio 0
	s_setprio 1
	v_mfma_f32_16x16x128_f8f6f4 v[184:187], v[16:23], v[32:39], v[184:187]
	v_mfma_f32_16x16x128_f8f6f4 v[180:183], v[24:31], v[32:39], v[180:183]
	v_mfma_f32_16x16x128_f8f6f4 v[172:175], v[16:23], v[40:47], v[172:175]
	v_mfma_f32_16x16x128_f8f6f4 v[164:167], v[24:31], v[40:47], v[164:167]
	v_mfma_f32_16x16x128_f8f6f4 v[156:159], v[16:23], v[48:55], v[156:159]
	v_mfma_f32_16x16x128_f8f6f4 v[148:151], v[24:31], v[48:55], v[148:151]
	v_mfma_f32_16x16x128_f8f6f4 v[140:143], v[16:23], v[56:63], v[140:143]
	v_mfma_f32_16x16x128_f8f6f4 v[132:135], v[24:31], v[56:63], v[132:135]
	s_setprio 0
	s_barrier
	s_mov_b32 m0, s58
	ds_read_b128 v[32:35], v200 offset:49152
	ds_read_b128 v[40:43], v200 offset:51200
	ds_read_b128 v[36:39], v199 offset:49152
	ds_read_b128 v[44:47], v199 offset:51200
	ds_read_b128 v[48:51], v200 offset:53248
	ds_read_b128 v[56:59], v200 offset:55296
	ds_read_b128 v[52:55], v199 offset:53248
	ds_read_b128 v[60:63], v199 offset:55296
	buffer_load_dwordx4 v203, s[8:11], s15 offen lds
	s_mov_b32 m0, s59
	s_add_i32 s7, s7, 0x40080
	buffer_load_dwordx4 v201, s[8:11], s15 offen lds
	s_mov_b32 m0, s62
	s_nop 0
	buffer_load_dwordx4 v203, s[8:11], s7 offen lds
	s_mov_b32 m0, s63
	s_nop 0
	buffer_load_dwordx4 v201, s[8:11], s7 offen lds
	s_mov_b32 m0, s60
	s_nop 0
	buffer_load_dwordx4 v64, s[16:19], s6 offen lds
	s_mov_b32 m0, s61
	s_nop 0
	buffer_load_dwordx4 v65, s[16:19], s6 offen lds
	s_waitcnt vmcnt(8)
	s_waitcnt lgkmcnt(0)
	s_barrier
	s_setprio 1
	s_waitcnt lgkmcnt(5)
	v_mfma_f32_16x16x128_f8f6f4 v[128:131], v[0:7], v[32:39], v[128:131]
	v_mfma_f32_16x16x128_f8f6f4 v[120:123], v[8:15], v[32:39], v[120:123]
	s_waitcnt lgkmcnt(4)
	v_mfma_f32_16x16x128_f8f6f4 v[112:115], v[0:7], v[40:47], v[112:115]
	v_mfma_f32_16x16x128_f8f6f4 v[104:107], v[8:15], v[40:47], v[104:107]
	s_waitcnt lgkmcnt(1)
	v_mfma_f32_16x16x128_f8f6f4 v[96:99], v[0:7], v[48:55], v[96:99]
	v_mfma_f32_16x16x128_f8f6f4 v[88:91], v[8:15], v[48:55], v[88:91]
	s_waitcnt lgkmcnt(0)
	v_mfma_f32_16x16x128_f8f6f4 v[80:83], v[0:7], v[56:63], v[80:83]
	v_mfma_f32_16x16x128_f8f6f4 v[72:75], v[8:15], v[56:63], v[72:75]
	s_setprio 0
	s_setprio 1
	v_mfma_f32_16x16x128_f8f6f4 v[124:127], v[16:23], v[32:39], v[124:127]
	v_mfma_f32_16x16x128_f8f6f4 v[116:119], v[24:31], v[32:39], v[116:119]
	v_mfma_f32_16x16x128_f8f6f4 v[108:111], v[16:23], v[40:47], v[108:111]
	v_mfma_f32_16x16x128_f8f6f4 v[100:103], v[24:31], v[40:47], v[100:103]
	v_mfma_f32_16x16x128_f8f6f4 v[92:95], v[16:23], v[48:55], v[92:95]
	v_mfma_f32_16x16x128_f8f6f4 v[84:87], v[24:31], v[48:55], v[84:87]
	v_mfma_f32_16x16x128_f8f6f4 v[76:79], v[16:23], v[56:63], v[76:79]
	v_mfma_f32_16x16x128_f8f6f4 v[68:71], v[24:31], v[56:63], v[68:71]
	s_setprio 0
	s_barrier
	s_addk_i32 s82, 0x100
	s_cmp_gt_u32 s77, 13
	s_cbranch_scc1 .LBB0_2479
	s_mov_b32 s77, s14
	s_branch .LBB0_2454

	.amdhsa_kernel _Z8mega_fwd4Args
		.amdhsa_group_segment_fixed_size 0
		.amdhsa_private_segment_fixed_size 0
		.amdhsa_kernarg_size 520
		.amdhsa_user_sgpr_count 2
		.amdhsa_user_sgpr_dispatch_ptr 0
		.amdhsa_user_sgpr_queue_ptr 0
		.amdhsa_user_sgpr_kernarg_segment_ptr 1
		.amdhsa_user_sgpr_dispatch_id 0
		.amdhsa_user_sgpr_kernarg_preload_length 0
		.amdhsa_user_sgpr_kernarg_preload_offset 0
		.amdhsa_user_sgpr_private_segment_size 0
		.amdhsa_uses_dynamic_stack 0
		.amdhsa_enable_private_segment 0
		.amdhsa_system_sgpr_workgroup_id_x 1
		.amdhsa_system_sgpr_workgroup_id_y 0
		.amdhsa_system_sgpr_workgroup_id_z 0
		.amdhsa_system_sgpr_workgroup_info 0
		.amdhsa_system_vgpr_workitem_id 0
		.amdhsa_next_free_vgpr 256
		.amdhsa_next_free_sgpr 101
		.amdhsa_accum_offset 256
		.amdhsa_reserve_vcc 1
		.amdhsa_float_round_mode_32 0
		.amdhsa_float_round_mode_16_64 0
		.amdhsa_float_denorm_mode_32 3
		.amdhsa_float_denorm_mode_16_64 3
		.amdhsa_dx10_clamp 1
		.amdhsa_ieee_mode 1
		.amdhsa_fp16_overflow 0
		.amdhsa_tg_split 0
		.amdhsa_exception_fp_ieee_invalid_op 0
		.amdhsa_exception_fp_denorm_src 0
		.amdhsa_exception_fp_ieee_div_zero 0
		.amdhsa_exception_fp_ieee_overflow 0
		.amdhsa_exception_fp_ieee_underflow 0
		.amdhsa_exception_fp_ieee_inexact 0
		.amdhsa_exception_int_div_zero 0
	.end_amdhsa_kernel

amdhsa.kernels:
  - .agpr_count:     0
    .args:
      - .offset:         0
        .size:           264
        .value_kind:     by_value
      - .offset:         264
        .size:           4
        .value_kind:     hidden_block_count_x
      - .offset:         268
        .size:           4
        .value_kind:     hidden_block_count_y
      - .offset:         272
        .size:           4
        .value_kind:     hidden_block_count_z
      - .offset:         276
        .size:           2
        .value_kind:     hidden_group_size_x
      - .offset:         278
        .size:           2
        .value_kind:     hidden_group_size_y
      - .offset:         280
        .size:           2
        .value_kind:     hidden_group_size_z
      - .offset:         282
        .size:           2
        .value_kind:     hidden_remainder_x
      - .offset:         284
        .size:           2
        .value_kind:     hidden_remainder_y
      - .offset:         286
        .size:           2
        .value_kind:     hidden_remainder_z
      - .offset:         304
        .size:           8
        .value_kind:     hidden_global_offset_x
      - .offset:         312
        .size:           8
        .value_kind:     hidden_global_offset_y
      - .offset:         320
        .size:           8
        .value_kind:     hidden_global_offset_z
      - .offset:         328
        .size:           2
        .value_kind:     hidden_grid_dims
      - .offset:         384
        .size:           4
        .value_kind:     hidden_dynamic_lds_size
    .group_segment_fixed_size: 0
    .kernarg_segment_align: 8
    .kernarg_segment_size: 520
    .language:       OpenCL C
    .language_version:
      - 2
      - 0
    .max_flat_workgroup_size: 512
    .name:           _Z8mega_fwd4Args
    .private_segment_fixed_size: 0
    .sgpr_count:     107
    .sgpr_spill_count: 93
    .symbol:         _Z8mega_fwd4Args.kd
    .uniform_work_group_size: 1
    .uses_dynamic_stack: false
    .vgpr_count:     256
    .vgpr_spill_count: 0
    .wavefront_size: 64
